# P12: nt cache policy on the weight (B operand) LDS-DMA loads of the up GEMM, on top of previous best
# baseline (speedup 1.0000x reference)
; __device__ __forceinline__ int lane_id_now() { unsigned z = 0u; asm volatile("" : "+v"(z)); return (int)__builtin_amdgcn_mbcnt_hi(~0u, __builtin_amdgcn_mbcnt_lo(~0u, z)); }
; #define PG8_STAGE(bufoff, gbase, voff) do { _Pragma("unroll") for (int _i = 0; _i < 2; ++_i) \
;         __builtin_amdgcn_global_load_lds((const unsigned*)((const char*)(gbase) + (voff)[_i]), (PG8_LAS unsigned*)(lds + (bufoff) + ldsw + _i * 8192), 16, 0, 0); } while (0)
; #define PG8_WAIT_V(n) asm volatile("s_waitcnt vmcnt(" #n ")" ::: "memory")
; #define PG8_BAR __builtin_amdgcn_s_barrier()
;     __device__ __forceinline__ bool next(int i, Unit& u) const { const int L = i * G + c; if (L >= NB * nN) return false; u.z = L / nN; u.pn = L % nN; u.pm = i; return true; }
; template <class Epi, class Sched, bool ALIGN_EPI = false, bool SP2 = false>
; __device__ __forceinline__ void gemm_phase(PG8_LAS unsigned char* lds, const Geo geo, const Sched& S, const Epi& E, const int wave_) {
;     ...
;     PG8_STAGE(PG8_SB(1, 0), cB + kstep, voffB); PG8_STAGE(PG8_SA(1, 0), cA + kstep, c0); PG8_STAGE(PG8_SB(1, 1), cB + hstepB + kstep, voffB);
;     PG8_WAIT_V(6); PG8_BAR;
;     for (;;) {
;         const bool has_next = S.next(ui + 1, nxt);
;         const char* nA = cA; const char* nB = cB; if (has_next) S.ptrs(nxt, nA, nB);
;         const bool h1 = S.half1(cur);
;         for (int t = 0; t < nt; t += 2) {
;     __device__ __forceinline__ void convert_share() const {
;         const int lane = lane_id_now(), gw = c * NWAVES + wave, NGW = G * NWAVES;
;         constexpr int NIT = E * (FF / 128) * (D / 32);
;         TSTREAM(NIT, dec_dn, TI8L_NT, TI8S_NT);
;     }
;     __device__ __forceinline__ void done(const Unit& u) const { if (u.pm == (c & 7)) convert_share(); }
.LBB0_1517:
	s_add_u32 s63, s78, 0x57dc8000
	s_addc_u32 s64, s79, 0
	s_add_u32 s14, s78, 0x6d7c8000
	s_addc_u32 s15, s79, 0
	s_add_u32 s93, s78, 0x23dc8000
	s_addc_u32 s9, s79, 0
	s_lshl_b32 s13, s0, 6
	s_lshl_b32 s26, s0, 13
	s_lshl_b32 s0, s1, 5
	s_and_b32 s20, s0, 0x60
	s_lshl_b32 s4, s20, 7
	s_add_i32 s70, s31, 0x18000
	s_mov_b64 s[16:17], 0x80
	s_add_i32 s72, s31, 0x1a000
	v_lshl_add_u64 v[2:3], v[2:3], 0, s[16:17]
	s_mov_b32 m0, s70
	s_add_u32 s18, s78, 0x67dc8080
	s_waitcnt vmcnt(2)
	s_barrier
	global_load_lds_dwordx4 v[2:3], off nt
	v_lshl_add_u64 v[0:1], v[0:1], 0, s[16:17]
	s_mov_b32 m0, s72
	s_addc_u32 s19, s79, 0
	s_add_i32 s74, s31, 0x8000
	s_add_i32 s82, s31, 0xa000
	global_load_lds_dwordx4 v[0:1], off nt
	v_lshl_add_u64 v[0:1], s[18:19], 0, v[64:65]
	s_mov_b32 m0, s74
	s_add_u32 s0, s6, 0x400080
	global_load_lds_dwordx4 v[0:1], off nt
	v_lshl_add_u64 v[0:1], s[18:19], 0, v[200:201]
	s_mov_b32 m0, s82
	s_addc_u32 s1, s7, 0
	s_add_i32 s95, s31, 0x1c000
	global_load_lds_dwordx4 v[0:1], off nt
	v_lshl_add_u64 v[0:1], s[0:1], 0, v[196:197]
	s_mov_b32 m0, s95
	s_add_i32 s97, s31, 0x1e000
	global_load_lds_dwordx4 v[0:1], off nt
	v_lshl_add_u64 v[0:1], s[0:1], 0, v[198:199]
	s_mov_b32 m0, s97
	s_add_i32 s4, s4, 0
	global_load_lds_dwordx4 v[0:1], off nt
	s_cmpk_lt_u32 s2, 0x100
	s_cselect_b64 s[24:25], -1, 0
	s_and_b32 s0, s92, 7
	v_writelane_b32 v254, s0, 10
	s_lshl_b32 s0, s92, 3
	v_readlane_b32 s3, v254, 60
	s_add_i32 s2, s3, s0
	s_lshl_b32 s22, s83, 3
	s_cmp_lt_i32 s2, 0x8000
	v_writelane_b32 v255, s0, 4
	s_cselect_b64 s[0:1], -1, 0
	v_writelane_b32 v254, s0, 26
	v_and_b32_e32 v218, 15, v4
	v_bfe_u32 v219, v4, 4, 2
	v_writelane_b32 v254, s1, 27
	s_ashr_i32 s0, s2, 31
	s_lshr_b32 s0, s0, 22
	v_lshlrev_b32_e32 v4, 2, v4
	s_add_i32 s1, s2, s0
	v_lshlrev_b32_e32 v5, 4, v219
	v_lshlrev_b32_e32 v6, 6, v218
	v_and_b32_e32 v4, 32, v4
	s_ashr_i32 s0, s1, 10
	s_and_b32 s1, s1, 0xfffffc00
	v_bitop3_b32 v4, v6, v4, v5 bitop3:0x36
	s_sub_i32 s1, s2, s1
	v_add_u32_e32 v0, s4, v4
	s_ashr_i32 s4, s1, 31
	s_lshr_b32 s4, s4, 26
	s_add_i32 s8, s1, s4
	s_and_b32 s4, s8, 0x7ffffc0
	s_sub_i32 s12, s1, s4
	s_ashr_i32 s1, s0, 31
	v_readlane_b32 s84, v254, 2
	s_lshl_b64 s[4:5], s[0:1], 22
	s_lshl_b64 s[0:1], s[0:1], 24
	v_readlane_b32 s86, v254, 4
	v_readlane_b32 s88, v254, 6
	v_readlane_b32 s87, v254, 5
	s_mov_b32 s88, s13
	s_add_u32 s13, s86, s0
	s_addc_u32 s23, s87, s1
	s_lshl_b32 s0, s8, 1
	s_and_b32 s0, s0, 0xffffff80
	s_ashr_i32 s1, s0, 31
	v_readlane_b32 s90, v254, 8
	v_readlane_b32 s91, v254, 9
	s_mov_b32 s87, s9
	s_lshl_b64 s[8:9], s[0:1], 13
	s_mov_b64 s[90:91], s[24:25]
	s_add_u32 s24, s13, s8
	s_addc_u32 s23, s23, s9
	s_lshl_b32 s8, s12, 5
	s_ashr_i32 s9, s8, 31
	s_lshl_b64 s[12:13], s[8:9], 2
	s_add_u32 s12, s24, s12
	s_addc_u32 s13, s23, s13
	v_writelane_b32 v255, s12, 5
	s_waitcnt vmcnt(6)
	v_add_u32_e32 v1, 0, v4
	v_readlane_b32 s85, v254, 3
	v_writelane_b32 v255, s13, 6
	s_add_u32 s12, s63, s4
	s_addc_u32 s13, s64, s5
	s_lshl_b64 s[4:5], s[8:9], 11
	s_add_u32 s4, s12, s4
	s_addc_u32 s5, s13, s5
	s_add_u32 s0, s4, s0
	s_addc_u32 s1, s5, s1
	v_writelane_b32 v255, s0, 7
	v_readlane_b32 s89, v254, 7
	s_mov_b32 s69, 0x18000
	v_writelane_b32 v255, s1, 8
	s_add_i32 s0, s22, s2
	s_cmp_lt_i32 s0, 0x8000
	s_cselect_b64 s[0:1], -1, 0
	v_writelane_b32 v255, s0, 9
	s_lshl_b32 s29, s83, 4
	s_mov_b32 s71, 0x1a000
	s_mov_b32 s73, 0x8000
	s_mov_b32 s75, 0xa000
	s_mov_b32 s94, 0x1c000
	s_mov_b32 s96, 0x1e000
	v_add_u32_e32 v201, 0x10000, v0
	v_add_u32_e32 v220, 0x10400, v0
	v_add_u32_e32 v221, 0x10800, v0
	v_add_u32_e32 v222, 0x10c00, v0
	v_add_u32_e32 v223, 0x14000, v0
	v_add_u32_e32 v224, 0x14400, v0
	v_add_u32_e32 v225, 0x14800, v0
	v_add_u32_e32 v226, 0x14c00, v0
	v_add_u32_e32 v227, 0x18000, v0
	v_add_u32_e32 v228, 0x18400, v0
	v_add_u32_e32 v229, 0x18800, v0
	v_add_u32_e32 v230, 0x18c00, v0
	v_add_u32_e32 v231, 0x1c000, v0
	v_add_u32_e32 v232, 0x1c400, v0
	v_add_u32_e32 v233, 0x1c800, v0
	v_add_u32_e32 v234, 0x1cc00, v0
	s_mov_b32 s89, s20
	v_writelane_b32 v255, s1, 10
	s_add_i32 s28, s3, s29
	s_add_i32 s12, s3, s22
	s_mov_b32 s13, 0xc000
	s_mov_b32 s22, 0xe000
	s_mov_b32 s23, 0xc0e00000
	s_mov_b32 s24, 0xc3e00000
	s_mov_b32 s30, 0x43800000
	s_movk_i32 s25, 0x1000
	v_add_u32_e32 v235, s26, v1
	v_mov_b32_e32 v236, 0x40e00000
	v_mov_b32_e32 v237, 0x43e00000
	v_mov_b32_e32 v240, v64
	s_mov_b32 s26, 0
	v_readlane_b32 s85, v254, 58
	v_readlane_b32 s86, v254, 61
	s_barrier
	s_branch .LBB0_1520

; #define PG8_STAGE(bufoff, gbase, voff) do { _Pragma("unroll") for (int _i = 0; _i < 2; ++_i) \
;         __builtin_amdgcn_global_load_lds((const unsigned*)((const char*)(gbase) + (voff)[_i]), (PG8_LAS unsigned*)(lds + (bufoff) + ldsw + _i * 8192), 16, 0, 0); } while (0)
; #define PG8_WAIT_V(n) asm volatile("s_waitcnt vmcnt(" #n ")" ::: "memory")
; #define PG8_WAIT_L(n) asm volatile("s_waitcnt lgkmcnt(" #n ")" ::: "memory")
; #define PG8_BAR __builtin_amdgcn_s_barrier()
; #define PG8_SCHED __builtin_amdgcn_sched_barrier(0)
; template <class Epi, class Sched, bool ALIGN_EPI = false, bool SP2 = false>
; __device__ __forceinline__ void gemm_phase(PG8_LAS unsigned char* lds, const Geo geo, const Sched& S, const Epi& E, const int wave_) {
;     ...
;             PG8_LDB(B0, 0, 0); PG8_LDB(B1, 0, 1); PG8_SCHED; PG8_LDA(At, 0, 0); PG8_STAGE(PG8_SA(1, 1), a1 + hstepA, c1);
;             PG8_WAIT_V(8); PG8_WAIT_L(0); PG8_BAR; PG8_MMA(0, 0, At, B0); PG8_MMA(0, 1, At, B1); PG8_BAR; PG8_SCHED;
;             PG8_LDA(At, 0, 1); PG8_STAGE(PG8_SB(0, 0), b2, voffB); PG8_STAGE(PG8_SB(0, 1), b2 + hstepB, voffB); PG8_STAGE(PG8_SA(0, 0), a2, s0);
;             PG8_WAIT_V(8); PG8_WAIT_L(0); PG8_BAR; if (h1) { PG8_MMA(1, 0, At, B0); PG8_MMA(1, 1, At, B1); } PG8_BAR; PG8_SCHED;
.LBB0_1528:
	ds_read_b128 v[16:19], v201
	ds_read_b128 v[20:23], v220
	ds_read_b128 v[24:27], v221
	ds_read_b128 v[28:31], v222
	ds_read_b128 v[0:3], v223
	ds_read_b128 v[4:7], v224
	ds_read_b128 v[8:11], v225
	ds_read_b128 v[12:15], v226
	s_add_u32 s8, s78, s44
	s_addc_u32 s9, s79, s45
	s_add_u32 s46, s8, 0x67dc8100
	s_addc_u32 s47, s9, 0
	s_and_b64 s[8:9], s[6:7], exec
	s_cselect_b32 s49, s11, s47
	s_cselect_b32 s48, s10, s46
	s_add_u32 s46, s39, s44
	s_addc_u32 s47, s66, s45
	s_and_b64 s[8:9], s[6:7], exec
	s_cselect_b32 s47, s37, s47
	s_cselect_b32 s46, s36, s46
	v_cndmask_b32_e64 v64, v240, v203, s[6:7]
	v_cndmask_b32_e64 v66, v200, v238, s[6:7]
	v_lshl_add_u64 v[210:211], v[208:209], 0, s[44:45]
	s_add_i32 m0, s31, 0xc000
	s_waitcnt lgkmcnt(0)
	ds_read_b128 v[32:35], v235
	ds_read_b128 v[36:39], v235 offset:1024
	ds_read_b128 v[40:43], v235 offset:2048
	ds_read_b128 v[44:47], v235 offset:3072
	ds_read_b128 v[48:51], v235 offset:4096
	ds_read_b128 v[52:55], v235 offset:5120
	ds_read_b128 v[56:59], v235 offset:6144
	ds_read_b128 v[60:63], v235 offset:7168
	global_load_lds_dwordx4 v[210:211], off nt
	v_lshl_add_u64 v[210:211], v[206:207], 0, s[44:45]
	s_add_i32 m0, s31, 0xe000
	s_nop 0
	global_load_lds_dwordx4 v[210:211], off nt
	s_waitcnt vmcnt(8)
	s_waitcnt lgkmcnt(0)
	s_barrier
	s_setprio 1
	s_waitcnt lgkmcnt(0)
	v_mfma_f32_16x16x128_f8f6f4 v[192:195], v[16:23], v[32:39], v[192:195]
	v_mfma_f32_16x16x128_f8f6f4 v[184:187], v[24:31], v[32:39], v[184:187]
	v_mfma_f32_16x16x128_f8f6f4 v[176:179], v[16:23], v[40:47], v[176:179]
	v_mfma_f32_16x16x128_f8f6f4 v[168:171], v[24:31], v[40:47], v[168:171]
	v_mfma_f32_16x16x128_f8f6f4 v[160:163], v[16:23], v[48:55], v[160:163]
	v_mfma_f32_16x16x128_f8f6f4 v[152:155], v[24:31], v[48:55], v[152:155]
	v_mfma_f32_16x16x128_f8f6f4 v[144:147], v[16:23], v[56:63], v[144:147]
	v_mfma_f32_16x16x128_f8f6f4 v[136:139], v[24:31], v[56:63], v[136:139]
	s_setprio 0
	s_setprio 1
	v_mfma_f32_16x16x128_f8f6f4 v[188:191], v[0:7], v[32:39], v[188:191]
	v_mfma_f32_16x16x128_f8f6f4 v[180:183], v[8:15], v[32:39], v[180:183]
	v_mfma_f32_16x16x128_f8f6f4 v[172:175], v[0:7], v[40:47], v[172:175]
	v_mfma_f32_16x16x128_f8f6f4 v[164:167], v[8:15], v[40:47], v[164:167]
	v_mfma_f32_16x16x128_f8f6f4 v[156:159], v[0:7], v[48:55], v[156:159]
	v_mfma_f32_16x16x128_f8f6f4 v[148:151], v[8:15], v[48:55], v[148:151]
	v_mfma_f32_16x16x128_f8f6f4 v[140:143], v[0:7], v[56:63], v[140:143]
	v_mfma_f32_16x16x128_f8f6f4 v[132:135], v[8:15], v[56:63], v[132:135]
	s_setprio 0
	s_barrier
	s_mov_b32 m0, s41
	v_lshl_add_u64 v[210:211], s[46:47], 0, v[196:197]
	s_add_u32 s8, s46, 0x400000
	ds_read_b128 v[56:59], v235 offset:16384
	ds_read_b128 v[60:63], v235 offset:17408
	ds_read_b128 v[48:51], v235 offset:18432
	ds_read_b128 v[52:55], v235 offset:19456
	ds_read_b128 v[40:43], v235 offset:20480
	ds_read_b128 v[44:47], v235 offset:21504
	ds_read_b128 v[32:35], v235 offset:22528
	ds_read_b128 v[36:39], v235 offset:23552
	global_load_lds_dwordx4 v[210:211], off nt
	v_lshl_add_u64 v[212:213], s[46:47], 0, v[198:199]
	s_mov_b32 m0, s50
	s_addc_u32 s9, s47, 0
	global_load_lds_dwordx4 v[212:213], off nt
	v_lshl_add_u64 v[244:245], s[8:9], 0, v[196:197]
	s_mov_b32 m0, s51
	v_cndmask_b32_e64 v67, 0, 1, s[4:5]
	global_load_lds_dwordx4 v[244:245], off nt
	v_lshl_add_u64 v[244:245], s[8:9], 0, v[198:199]
	s_mov_b32 m0, s52
	v_cmp_ne_u32_e64 s[8:9], 1, v67
	global_load_lds_dwordx4 v[244:245], off nt
	s_mov_b32 m0, s31
	s_andn2_b64 vcc, exec, s[4:5]
	global_load_lds_dwordx4 v64, s[48:49]
	s_mov_b32 m0, s53
	s_nop 0
	global_load_lds_dwordx4 v66, s[48:49]
	s_waitcnt vmcnt(8)
	s_waitcnt lgkmcnt(0)
	s_barrier
	s_cbranch_vccnz .LBB0_1530
	s_setprio 1
	s_waitcnt lgkmcnt(0)
	v_mfma_f32_16x16x128_f8f6f4 v[128:131], v[16:23], v[56:63], v[128:131]
	v_mfma_f32_16x16x128_f8f6f4 v[120:123], v[24:31], v[56:63], v[120:123]
	v_mfma_f32_16x16x128_f8f6f4 v[112:115], v[16:23], v[48:55], v[112:115]
	v_mfma_f32_16x16x128_f8f6f4 v[104:107], v[24:31], v[48:55], v[104:107]
	v_mfma_f32_16x16x128_f8f6f4 v[96:99], v[16:23], v[40:47], v[96:99]
	v_mfma_f32_16x16x128_f8f6f4 v[88:91], v[24:31], v[40:47], v[88:91]
	v_mfma_f32_16x16x128_f8f6f4 v[80:83], v[16:23], v[32:39], v[80:83]
	v_mfma_f32_16x16x128_f8f6f4 v[72:75], v[24:31], v[32:39], v[72:75]
	s_setprio 0
	s_setprio 1
	v_mfma_f32_16x16x128_f8f6f4 v[124:127], v[0:7], v[56:63], v[124:127]
	v_mfma_f32_16x16x128_f8f6f4 v[116:119], v[8:15], v[56:63], v[116:119]
	v_mfma_f32_16x16x128_f8f6f4 v[108:111], v[0:7], v[48:55], v[108:111]
	v_mfma_f32_16x16x128_f8f6f4 v[100:103], v[8:15], v[48:55], v[100:103]
	v_mfma_f32_16x16x128_f8f6f4 v[92:95], v[0:7], v[40:47], v[92:95]
	v_mfma_f32_16x16x128_f8f6f4 v[84:87], v[8:15], v[40:47], v[84:87]
	v_mfma_f32_16x16x128_f8f6f4 v[76:79], v[0:7], v[32:39], v[76:79]
	v_mfma_f32_16x16x128_f8f6f4 v[68:71], v[8:15], v[32:39], v[68:71]
	s_setprio 0
; #define PG8_STAGE(bufoff, gbase, voff) do { _Pragma("unroll") for (int _i = 0; _i < 2; ++_i) \
;         __builtin_amdgcn_global_load_lds((const unsigned*)((const char*)(gbase) + (voff)[_i]), (PG8_LAS unsigned*)(lds + (bufoff) + ldsw + _i * 8192), 16, 0, 0); } while (0)
; #define PG8_WAIT_V(n) asm volatile("s_waitcnt vmcnt(" #n ")" ::: "memory")
; #define PG8_WAIT_L(n) asm volatile("s_waitcnt lgkmcnt(" #n ")" ::: "memory")
; #define PG8_BAR __builtin_amdgcn_s_barrier()
; #define PG8_SCHED __builtin_amdgcn_sched_barrier(0)
; template <class Epi, class Sched, bool ALIGN_EPI = false, bool SP2 = false>
; __device__ __forceinline__ void gemm_phase(PG8_LAS unsigned char* lds, const Geo geo, const Sched& S, const Epi& E, const int wave_) {
;     ...
;             PG8_LDB(B0, 1, 0); PG8_LDB(B1, 1, 1); PG8_SCHED; PG8_LDA(At, 1, 0); PG8_STAGE(PG8_SA(0, 1), a2 + hstepA, s1);
;             PG8_WAIT_V(8); PG8_WAIT_L(0); PG8_BAR; PG8_MMA(0, 0, At, B0); PG8_MMA(0, 1, At, B1); PG8_BAR; PG8_SCHED;
;             PG8_LDA(At, 1, 1); PG8_STAGE(PG8_SB(1, 0), b3, voffB); PG8_STAGE(PG8_SB(1, 1), b3 + hstepB, voffB); PG8_STAGE(PG8_SA(1, 0), a3, s0);
;             PG8_WAIT_V(8); PG8_WAIT_L(0); PG8_BAR; if (h1) { PG8_MMA(1, 0, At, B0); PG8_MMA(1, 1, At, B1); } PG8_BAR; PG8_SCHED;
.LBB0_1530:
	v_mov_b32_e32 v67, v65
	v_lshl_add_u64 v[244:245], s[48:49], 0, v[64:65]
	v_lshl_add_u64 v[66:67], s[48:49], 0, v[66:67]
	v_cndmask_b32_e64 v64, v202, v205, s[6:7]
	v_cndmask_b32_e64 v243, v204, v239, s[6:7]
	s_barrier
	ds_read_b128 v[16:19], v227
	ds_read_b128 v[20:23], v228
	ds_read_b128 v[24:27], v229
	ds_read_b128 v[28:31], v230
	ds_read_b128 v[0:3], v231
	ds_read_b128 v[4:7], v232
	ds_read_b128 v[8:11], v233
	ds_read_b128 v[12:15], v234
	s_mov_b32 m0, s54
	s_waitcnt lgkmcnt(0)
	ds_read_b128 v[32:35], v235 offset:32768
	ds_read_b128 v[36:39], v235 offset:33792
	ds_read_b128 v[40:43], v235 offset:34816
	ds_read_b128 v[44:47], v235 offset:35840
	ds_read_b128 v[48:51], v235 offset:36864
	ds_read_b128 v[52:55], v235 offset:37888
	ds_read_b128 v[56:59], v235 offset:38912
	ds_read_b128 v[60:63], v235 offset:39936
	global_load_lds_dwordx4 v64, s[48:49]
	s_mov_b32 m0, s55
	s_nop 0
	global_load_lds_dwordx4 v243, s[48:49]
	s_waitcnt vmcnt(8)
	s_waitcnt lgkmcnt(0)
	s_barrier
	s_setprio 1
	s_waitcnt lgkmcnt(0)
	v_mfma_f32_16x16x128_f8f6f4 v[192:195], v[16:23], v[32:39], v[192:195]
	v_mfma_f32_16x16x128_f8f6f4 v[184:187], v[24:31], v[32:39], v[184:187]
	v_mfma_f32_16x16x128_f8f6f4 v[176:179], v[16:23], v[40:47], v[176:179]
	v_mfma_f32_16x16x128_f8f6f4 v[168:171], v[24:31], v[40:47], v[168:171]
	v_mfma_f32_16x16x128_f8f6f4 v[160:163], v[16:23], v[48:55], v[160:163]
	v_mfma_f32_16x16x128_f8f6f4 v[152:155], v[24:31], v[48:55], v[152:155]
	v_mfma_f32_16x16x128_f8f6f4 v[144:147], v[16:23], v[56:63], v[144:147]
	v_mfma_f32_16x16x128_f8f6f4 v[136:139], v[24:31], v[56:63], v[136:139]
	s_setprio 0
	s_setprio 1
	v_mfma_f32_16x16x128_f8f6f4 v[188:191], v[0:7], v[32:39], v[188:191]
	v_mfma_f32_16x16x128_f8f6f4 v[180:183], v[8:15], v[32:39], v[180:183]
	v_mfma_f32_16x16x128_f8f6f4 v[172:175], v[0:7], v[40:47], v[172:175]
	v_mfma_f32_16x16x128_f8f6f4 v[164:167], v[8:15], v[40:47], v[164:167]
	v_mfma_f32_16x16x128_f8f6f4 v[156:159], v[0:7], v[48:55], v[156:159]
	v_mfma_f32_16x16x128_f8f6f4 v[148:151], v[8:15], v[48:55], v[148:151]
	v_mfma_f32_16x16x128_f8f6f4 v[140:143], v[0:7], v[56:63], v[140:143]
	v_mfma_f32_16x16x128_f8f6f4 v[132:135], v[8:15], v[56:63], v[132:135]
	s_setprio 0
	s_barrier
	s_mov_b32 m0, s70
	v_lshl_add_u64 v[210:211], v[210:211], 0, s[16:17]
	s_add_u32 s6, s46, 0x400080
	ds_read_b128 v[56:59], v235 offset:49152
	ds_read_b128 v[60:63], v235 offset:50176
	ds_read_b128 v[48:51], v235 offset:51200
	ds_read_b128 v[52:55], v235 offset:52224
	ds_read_b128 v[40:43], v235 offset:53248
	ds_read_b128 v[44:47], v235 offset:54272
	ds_read_b128 v[32:35], v235 offset:55296
	ds_read_b128 v[36:39], v235 offset:56320
	global_load_lds_dwordx4 v[210:211], off nt
	v_lshl_add_u64 v[210:211], v[212:213], 0, s[16:17]
	s_mov_b32 m0, s72
	s_addc_u32 s7, s47, 0
	global_load_lds_dwordx4 v[210:211], off nt
	v_lshl_add_u64 v[210:211], s[6:7], 0, v[196:197]
	s_mov_b32 m0, s95
	v_lshl_add_u64 v[66:67], v[66:67], 0, s[16:17]
	global_load_lds_dwordx4 v[210:211], off nt
	v_lshl_add_u64 v[210:211], s[6:7], 0, v[198:199]
	s_mov_b32 m0, s97
	s_and_b64 vcc, exec, s[8:9]
	global_load_lds_dwordx4 v[210:211], off nt
	v_lshl_add_u64 v[210:211], v[244:245], 0, s[16:17]
	s_mov_b32 m0, s74
	s_nop 0
	global_load_lds_dwordx4 v[210:211], off nt
	s_mov_b32 m0, s82
	s_nop 0
	global_load_lds_dwordx4 v[66:67], off nt
	s_waitcnt vmcnt(8)
	s_waitcnt lgkmcnt(0)
	s_barrier
	s_cbranch_vccnz .LBB0_1525
	s_setprio 1
	s_waitcnt lgkmcnt(0)
	v_mfma_f32_16x16x128_f8f6f4 v[128:131], v[16:23], v[56:63], v[128:131]
	v_mfma_f32_16x16x128_f8f6f4 v[120:123], v[24:31], v[56:63], v[120:123]
	v_mfma_f32_16x16x128_f8f6f4 v[112:115], v[16:23], v[48:55], v[112:115]
	v_mfma_f32_16x16x128_f8f6f4 v[104:107], v[24:31], v[48:55], v[104:107]
	v_mfma_f32_16x16x128_f8f6f4 v[96:99], v[16:23], v[40:47], v[96:99]
	v_mfma_f32_16x16x128_f8f6f4 v[88:91], v[24:31], v[40:47], v[88:91]
	v_mfma_f32_16x16x128_f8f6f4 v[80:83], v[16:23], v[32:39], v[80:83]
	v_mfma_f32_16x16x128_f8f6f4 v[72:75], v[24:31], v[32:39], v[72:75]
	s_setprio 0
	s_setprio 1
	v_mfma_f32_16x16x128_f8f6f4 v[124:127], v[0:7], v[56:63], v[124:127]
	v_mfma_f32_16x16x128_f8f6f4 v[116:119], v[8:15], v[56:63], v[116:119]
	v_mfma_f32_16x16x128_f8f6f4 v[108:111], v[0:7], v[48:55], v[108:111]
	v_mfma_f32_16x16x128_f8f6f4 v[100:103], v[8:15], v[48:55], v[100:103]
	v_mfma_f32_16x16x128_f8f6f4 v[92:95], v[0:7], v[40:47], v[92:95]
	v_mfma_f32_16x16x128_f8f6f4 v[84:87], v[8:15], v[40:47], v[84:87]
	v_mfma_f32_16x16x128_f8f6f4 v[76:79], v[0:7], v[32:39], v[76:79]
	v_mfma_f32_16x16x128_f8f6f4 v[68:71], v[8:15], v[32:39], v[68:71]
	s_setprio 0
	s_branch .LBB0_1525
